# S7: S4 + s_setprio 3 for the 32 last-dispatched K1 blocks (stragglers sharing a CU with an older block)
# speedup vs baseline: 1.0074x; 1.0074x over previous
_Z12gemm1_kernelPKfS0_S0_PDv8_DF16_PDF16_S3_:
	s_cmp_lt_u32 s2, 0x100
	s_cbranch_scc1 .Lk1_noprio
	s_setprio 3
.Lk1_noprio:
	s_and_b32 s3, s2, 7
	s_ashr_i32 s2, s2, 3
	s_mul_hi_i32 s8, s2, 0x2aaaaaab
	s_lshr_b32 s9, s8, 31
	s_ashr_i32 s8, s8, 1
	s_mul_i32 s3, s3, 3
	s_add_i32 s8, s8, s9
	s_load_dwordx4 s[4:7], s[0:1], 0x0
	s_load_dwordx2 s[10:11], s[0:1], 0x10
	s_add_i32 s3, s3, s8
	s_mul_i32 s8, s8, 12
	v_bfe_u32 v85, v0, 6, 2
	s_sub_i32 s8, s2, s8
	v_lshlrev_b32_e32 v1, 5, v85
	s_ashr_i32 s9, s8, 31
	v_lshl_or_b32 v1, s3, 7, v1
	s_lshl_b64 s[2:3], s[8:9], 17
	v_bfe_u32 v18, v0, 3, 3
	v_lshlrev_b32_e32 v4, 5, v0
	v_and_b32_e32 v6, 0x100, v0
	v_or_b32_e32 v2, v1, v18
	s_waitcnt lgkmcnt(0)
	s_add_u32 s2, s6, s2
	v_and_b32_e32 v4, 0x1800, v4
	v_and_b32_e32 v84, 63, v0
	v_mov_b32_e32 v67, 0
	v_ashrrev_i32_e32 v3, 31, v2
	s_addc_u32 s3, s7, s3
	v_lshl_or_b32 v66, v6, 8, v4
	v_lshlrev_b64 v[2:3], 11, v[2:3]
	v_lshl_add_u64 v[4:5], s[2:3], 0, v[66:67]
	v_lshlrev_b32_e32 v66, 2, v84
	v_and_b32_e32 v78, 7, v0
	v_lshl_add_u64 v[68:69], v[4:5], 0, v[66:67]
	v_lshl_add_u64 v[2:3], s[4:5], 0, v[2:3]
	v_lshlrev_b32_e32 v4, 2, v6
	v_mov_b32_e32 v5, v67
	v_lshl_add_u64 v[2:3], v[2:3], 0, v[4:5]
	v_lshlrev_b32_e32 v4, 4, v78
	v_lshl_add_u64 v[70:71], v[2:3], 0, v[4:5]
	s_movk_i32 s4, 0x4000
	v_add_co_u32_e32 v72, vcc, s4, v70
	global_load_dwordx4 v[2:5], v[70:71], off
	s_nop 0
	v_addc_co_u32_e32 v73, vcc, 0, v71, vcc
	global_load_dwordx4 v[6:9], v[72:73], off
	s_mov_b32 s3, 0x8000
	global_load_dword v20, v[68:69], off
	global_load_dword v21, v[68:69], off offset:1792
	global_load_dword v22, v[68:69], off offset:1536
	global_load_dword v23, v[68:69], off offset:1280
	global_load_dword v24, v[68:69], off offset:1024
	global_load_dword v25, v[68:69], off offset:768
	global_load_dword v26, v[68:69], off offset:512
	global_load_dword v27, v[68:69], off offset:256
	v_add_co_u32_e32 v76, vcc, s3, v70
	v_and_b32_e32 v79, 31, v0
	s_nop 0
	v_addc_co_u32_e32 v77, vcc, 0, v71, vcc
	global_load_dwordx4 v[10:13], v[76:77], off
	s_mov_b32 s2, 0xc000
	v_lshrrev_b32_e32 v19, 6, v0
	v_mul_u32_u24_e32 v29, 0x50, v18
	v_lshl_or_b32 v18, s8, 7, v79
	v_add_co_u32_e32 v74, vcc, s2, v70
	v_mul_u32_u24_e32 v28, 0x1400, v19
	v_ashrrev_i32_e32 v19, 31, v18
	v_addc_co_u32_e32 v75, vcc, 0, v71, vcc
	v_lshl_add_u64 v[18:19], v[18:19], 2, s[10:11]
	global_load_dwordx4 v[14:17], v[74:75], off
	global_load_dword v80, v[18:19], off
	global_load_dword v83, v[18:19], off offset:128
	global_load_dword v81, v[18:19], off offset:256
	global_load_dword v82, v[18:19], off offset:384
	v_lshrrev_b32_e32 v86, 8, v0
	v_mov_b32_e32 v18, 0xa000
	s_movk_i32 s5, 0x2000
	v_lshl_add_u32 v32, v86, 13, v18
	v_add_co_u32_e32 v18, vcc, s5, v68
	global_load_dwordx4 v[62:65], v[70:71], off offset:128
	global_load_dwordx4 v[58:61], v[72:73], off offset:128
	global_load_dwordx4 v[54:57], v[76:77], off offset:128
	global_load_dwordx4 v[50:53], v[74:75], off offset:128
	v_addc_co_u32_e32 v19, vcc, 0, v69, vcc
	global_load_dword v91, v[18:19], off offset:1792
	global_load_dword v104, v[18:19], off offset:1536
	global_load_dword v105, v[18:19], off offset:1280
	global_load_dword v106, v[18:19], off offset:1024
	global_load_dword v107, v[18:19], off offset:768
	global_load_dword v108, v[18:19], off offset:512
	global_load_dword v109, v[18:19], off offset:256
	global_load_dword v110, v[18:19], off
	v_bfe_u32 v67, v0, 5, 1
	v_mul_u32_u24_e32 v30, 0x50, v79
	v_lshlrev_b32_e32 v31, 4, v67
	v_add3_u32 v89, v28, v30, v31
	v_lshl_or_b32 v88, v84, 4, v32
	s_waitcnt vmcnt(18)
	v_mov_b32_e32 v33, v3
	v_mov_b32_e32 v3, v5
	v_lshlrev_b32_e32 v5, 4, v0
	v_mov_b32_e32 v19, v8
	v_cvt_pk_f16_f32 v8, v20, v27
	v_and_b32_e32 v5, 0x800, v5
	v_lshlrev_b32_e32 v20, 10, v67
	v_or3_b32 v5, v32, v5, v20
	v_lshlrev_b32_e32 v20, 3, v0
	v_mov_b32_e32 v18, v9
	s_waitcnt vmcnt(17)
	v_mov_b32_e32 v35, v11
	v_cvt_pk_f16_f32 v11, v22, v21
	v_and_b32_e32 v20, 0x200, v20
	v_lshlrev_b32_e32 v21, 4, v79
	v_or3_b32 v87, v5, v20, v21
	v_or_b32_e32 v5, v28, v29
	v_mov_b32_e32 v34, v10
	v_cvt_pk_f16_f32 v10, v24, v23
	v_cvt_pk_f16_f32 v9, v26, v25
	v_lshl_add_u32 v90, v78, 3, v5
	v_cvt_pk_f16_f32 v3, v4, v3
	v_cvt_pk_f16_f32 v2, v2, v33
	v_cvt_pk_f16_f32 v5, v19, v18
	v_cvt_pk_f16_f32 v4, v6, v7
	s_waitcnt vmcnt(16)
	ds_write_b128 v87, v[8:11]
	ds_write2_b64 v90, v[2:3], v[4:5] offset1:80
	v_cvt_pk_f16_f32 v3, v12, v13
	v_cvt_pk_f16_f32 v2, v34, v35
	v_cvt_pk_f16_f32 v5, v16, v17
	v_cvt_pk_f16_f32 v4, v14, v15
	ds_write2_b64 v90, v[2:3], v[4:5] offset0:160 offset1:240
	v_add_co_u32_e32 v2, vcc, s4, v68
	global_load_dwordx4 v[34:37], v[70:71], off offset:256
	global_load_dwordx4 v[38:41], v[72:73], off offset:256
	global_load_dwordx4 v[42:45], v[76:77], off offset:256
	global_load_dwordx4 v[46:49], v[74:75], off offset:256
	v_addc_co_u32_e32 v3, vcc, 0, v69, vcc
	global_load_dword v111, v[2:3], off offset:1792
	global_load_dword v112, v[2:3], off offset:1536
	global_load_dword v113, v[2:3], off offset:1280
	global_load_dword v114, v[2:3], off offset:1024
	global_load_dword v115, v[2:3], off offset:768
	global_load_dword v116, v[2:3], off offset:512
	global_load_dword v117, v[2:3], off offset:256
	global_load_dword v118, v[2:3], off
	s_waitcnt lgkmcnt(0)
	s_barrier
	ds_read_b128 v[2:5], v89
	ds_read_b128 v[6:9], v88
	ds_read_b128 v[92:95], v89 offset:32
	ds_read_b128 v[10:13], v88 offset:1024
	s_waitcnt lgkmcnt(2)
	v_mfma_f32_32x32x16_f16 v[18:33], v[2:5], v[6:9], 0
	ds_read_b128 v[96:99], v88 offset:2048
	ds_read_b128 v[100:103], v88 offset:3072
	s_waitcnt vmcnt(12)
	s_movk_i32 s4, 0x6000
	s_waitcnt lgkmcnt(2)
	v_mfma_f32_32x32x16_f16 v[2:17], v[2:5], v[10:13], 0
	s_waitcnt lgkmcnt(1)
	v_mfma_f32_32x32x16_f16 v[18:33], v[92:95], v[96:99], v[18:33]
	v_mov_b32_e32 v96, v53
	v_mov_b32_e32 v97, v56
	v_mov_b32_e32 v98, v52
	v_mov_b32_e32 v99, v57
	s_waitcnt lgkmcnt(0)
	v_mfma_f32_32x32x16_f16 v[2:17], v[92:95], v[100:103], v[2:17]
	v_mov_b32_e32 v92, v60
	v_mov_b32_e32 v93, v63
	v_mov_b32_e32 v94, v62
	v_mov_b32_e32 v95, v61
	v_cvt_pk_f16_f32 v63, v104, v91
	v_cvt_pk_f16_f32 v62, v106, v105
	v_cvt_pk_f16_f32 v61, v108, v107
	v_cvt_pk_f16_f32 v60, v110, v109
	v_cvt_pk_f16_f32 v53, v64, v65
	v_cvt_pk_f16_f32 v52, v94, v93
	v_cvt_pk_f16_f32 v57, v92, v95
	v_cvt_pk_f16_f32 v56, v58, v59
	v_add_u32_e32 v91, 0x800, v90
	ds_write_b128 v87, v[60:63] offset:4096
	ds_write2_b64 v91, v[52:53], v[56:57] offset0:64 offset1:144
	v_cvt_pk_f16_f32 v53, v97, v99
	v_cvt_pk_f16_f32 v52, v54, v55
	v_cvt_pk_f16_f32 v55, v98, v96
	v_cvt_pk_f16_f32 v54, v50, v51
	v_add_u32_e32 v92, 0xc00, v90
	v_add_co_u32_e32 v94, vcc, s4, v68
	ds_write2_b64 v92, v[52:53], v[54:55] offset0:96 offset1:176
	s_nop 0
	v_addc_co_u32_e32 v95, vcc, 0, v69, vcc
	global_load_dwordx4 v[50:53], v[70:71], off offset:384
	global_load_dwordx4 v[54:57], v[72:73], off offset:384
	global_load_dwordx4 v[58:61], v[76:77], off offset:384
	global_load_dwordx4 v[62:65], v[74:75], off offset:384
	global_load_dword v93, v[94:95], off offset:1792
	global_load_dword v110, v[94:95], off offset:1536
	global_load_dword v119, v[94:95], off offset:1280
	global_load_dword v120, v[94:95], off offset:1024
	global_load_dword v121, v[94:95], off offset:768
	global_load_dword v122, v[94:95], off offset:512
	global_load_dword v123, v[94:95], off offset:256
	global_load_dword v124, v[94:95], off
	s_waitcnt lgkmcnt(0)
	s_barrier
	ds_read_b128 v[94:97], v89 offset:2560
	ds_read_b128 v[98:101], v88 offset:4096
	ds_read_b128 v[102:105], v89 offset:2592
	ds_read_b128 v[106:109], v88 offset:5120
	s_waitcnt lgkmcnt(2)
	v_mfma_f32_32x32x16_f16 v[18:33], v[94:97], v[98:101], v[18:33]
	s_waitcnt lgkmcnt(0)
	v_mfma_f32_32x32x16_f16 v[2:17], v[94:97], v[106:109], v[2:17]
	ds_read_b128 v[94:97], v88 offset:6144
	ds_read_b128 v[98:101], v88 offset:7168
	s_waitcnt vmcnt(12)
	s_waitcnt lgkmcnt(1)
	v_mfma_f32_32x32x16_f16 v[18:33], v[102:105], v[94:97], v[18:33]
	v_mov_b32_e32 v94, v37
	v_mov_b32_e32 v95, v39
	v_mov_b32_e32 v96, v36
	v_mov_b32_e32 v97, v38
	v_cvt_pk_f16_f32 v39, v112, v111
	v_cvt_pk_f16_f32 v38, v114, v113
	v_cvt_pk_f16_f32 v37, v116, v115
	v_cvt_pk_f16_f32 v36, v118, v117
	ds_write_b128 v87, v[36:39]
	v_cvt_pk_f16_f32 v37, v96, v94
	v_cvt_pk_f16_f32 v36, v34, v35
	v_cvt_pk_f16_f32 v35, v40, v41
	v_cvt_pk_f16_f32 v34, v97, v95
	ds_write2_b64 v90, v[36:37], v[34:35] offset1:80
	v_cvt_pk_f16_f32 v35, v44, v45
	v_cvt_pk_f16_f32 v34, v42, v43
	v_cvt_pk_f16_f32 v37, v48, v49
	v_cvt_pk_f16_f32 v36, v46, v47
	v_add_co_u32_e32 v94, vcc, s3, v68
	s_waitcnt lgkmcnt(2)
	v_mfma_f32_32x32x16_f16 v[2:17], v[102:105], v[98:101], v[2:17]
	ds_write2_b64 v90, v[34:35], v[36:37] offset0:160 offset1:240
	v_addc_co_u32_e32 v95, vcc, 0, v69, vcc
	global_load_dwordx4 v[34:37], v[70:71], off offset:512
	global_load_dwordx4 v[38:41], v[72:73], off offset:512
	global_load_dwordx4 v[42:45], v[76:77], off offset:512
	global_load_dwordx4 v[46:49], v[74:75], off offset:512
	global_load_dword v111, v[94:95], off offset:1792
	global_load_dword v112, v[94:95], off offset:1536
	global_load_dword v113, v[94:95], off offset:1280
	global_load_dword v114, v[94:95], off offset:1024
	global_load_dword v115, v[94:95], off offset:768
	global_load_dword v116, v[94:95], off offset:512
	global_load_dword v117, v[94:95], off offset:256
	global_load_dword v118, v[94:95], off
	s_waitcnt lgkmcnt(0)
	s_barrier
	ds_read_b128 v[94:97], v89
	ds_read_b128 v[98:101], v88
	ds_read_b128 v[102:105], v89 offset:32
	ds_read_b128 v[106:109], v88 offset:1024
	s_waitcnt lgkmcnt(2)
	v_mfma_f32_32x32x16_f16 v[18:33], v[94:97], v[98:101], v[18:33]
	s_mov_b32 s3, 0xa000
	s_waitcnt lgkmcnt(0)
	v_mfma_f32_32x32x16_f16 v[2:17], v[94:97], v[106:109], v[2:17]
	ds_read_b128 v[94:97], v88 offset:2048
	ds_read_b128 v[98:101], v88 offset:3072
	s_waitcnt vmcnt(12)
	s_waitcnt lgkmcnt(1)
	v_mfma_f32_32x32x16_f16 v[18:33], v[102:105], v[94:97], v[18:33]
	v_mov_b32_e32 v94, v51
	v_mov_b32_e32 v95, v61
	v_mov_b32_e32 v96, v63
	v_mov_b32_e32 v97, v60
	v_cvt_pk_f16_f32 v63, v110, v93
	v_cvt_pk_f16_f32 v61, v122, v121
	s_waitcnt lgkmcnt(0)
	v_mfma_f32_32x32x16_f16 v[2:17], v[102:105], v[98:101], v[2:17]
	v_mov_b32_e32 v98, v62
	v_cvt_pk_f16_f32 v62, v120, v119
	v_cvt_pk_f16_f32 v60, v124, v123
	v_cvt_pk_f16_f32 v51, v52, v53
	v_cvt_pk_f16_f32 v50, v50, v94
	v_cvt_pk_f16_f32 v53, v56, v57
	v_cvt_pk_f16_f32 v52, v54, v55
	ds_write_b128 v87, v[60:63] offset:4096
	ds_write2_b64 v91, v[50:51], v[52:53] offset0:64 offset1:144
	v_cvt_pk_f16_f32 v51, v97, v95
	v_cvt_pk_f16_f32 v50, v58, v59
	v_cvt_pk_f16_f32 v53, v64, v65
	v_cvt_pk_f16_f32 v52, v98, v96
	v_add_co_u32_e32 v94, vcc, s3, v68
	ds_write2_b64 v92, v[50:51], v[52:53] offset0:96 offset1:176
	s_nop 0
	v_addc_co_u32_e32 v95, vcc, 0, v69, vcc
	global_load_dwordx4 v[50:53], v[70:71], off offset:640
	global_load_dwordx4 v[54:57], v[72:73], off offset:640
	global_load_dwordx4 v[58:61], v[76:77], off offset:640
	global_load_dwordx4 v[62:65], v[74:75], off offset:640
	global_load_dword v93, v[94:95], off offset:1792
	global_load_dword v110, v[94:95], off offset:1536
	global_load_dword v119, v[94:95], off offset:1280
	global_load_dword v120, v[94:95], off offset:1024
	global_load_dword v121, v[94:95], off offset:768
	global_load_dword v122, v[94:95], off offset:512
	global_load_dword v123, v[94:95], off offset:256
	global_load_dword v124, v[94:95], off
	s_waitcnt lgkmcnt(0)
	s_barrier
	ds_read_b128 v[94:97], v89 offset:2560
	ds_read_b128 v[98:101], v88 offset:4096
	ds_read_b128 v[102:105], v89 offset:2592
	ds_read_b128 v[106:109], v88 offset:5120
	s_waitcnt lgkmcnt(2)
	v_mfma_f32_32x32x16_f16 v[18:33], v[94:97], v[98:101], v[18:33]
	s_waitcnt lgkmcnt(0)
	v_mfma_f32_32x32x16_f16 v[2:17], v[94:97], v[106:109], v[2:17]
	ds_read_b128 v[94:97], v88 offset:6144
	ds_read_b128 v[98:101], v88 offset:7168
	s_waitcnt vmcnt(12)
	s_waitcnt lgkmcnt(1)
	v_mfma_f32_32x32x16_f16 v[18:33], v[102:105], v[94:97], v[18:33]
	v_mov_b32_e32 v94, v41
	v_mov_b32_e32 v95, v40
	v_mov_b32_e32 v96, v35
	v_mov_b32_e32 v35, v37
	v_mov_b32_e32 v97, v42
	v_cvt_pk_f16_f32 v42, v114, v113
	s_waitcnt lgkmcnt(0)
	v_mfma_f32_32x32x16_f16 v[2:17], v[102:105], v[98:101], v[2:17]
	v_mov_b32_e32 v98, v43
	v_cvt_pk_f16_f32 v43, v112, v111
	v_cvt_pk_f16_f32 v41, v116, v115
	v_cvt_pk_f16_f32 v40, v118, v117
	v_cvt_pk_f16_f32 v35, v36, v35
	v_cvt_pk_f16_f32 v34, v34, v96
	v_cvt_pk_f16_f32 v37, v95, v94
	v_cvt_pk_f16_f32 v36, v38, v39
	ds_write_b128 v87, v[40:43]
	ds_write2_b64 v90, v[34:35], v[36:37] offset1:80
	v_cvt_pk_f16_f32 v35, v44, v45
	v_cvt_pk_f16_f32 v34, v97, v98
	v_cvt_pk_f16_f32 v37, v48, v49
	v_cvt_pk_f16_f32 v36, v46, v47
	v_add_co_u32_e32 v94, vcc, s2, v68
	ds_write2_b64 v90, v[34:35], v[36:37] offset0:160 offset1:240
	s_nop 0
	v_addc_co_u32_e32 v95, vcc, 0, v69, vcc
	global_load_dwordx4 v[34:37], v[70:71], off offset:768
	global_load_dwordx4 v[38:41], v[72:73], off offset:768
	global_load_dwordx4 v[42:45], v[76:77], off offset:768
	global_load_dwordx4 v[46:49], v[74:75], off offset:768
	global_load_dword v111, v[94:95], off offset:1792
	global_load_dword v112, v[94:95], off offset:1536
	global_load_dword v113, v[94:95], off offset:1280
	global_load_dword v114, v[94:95], off offset:1024
	global_load_dword v115, v[94:95], off offset:768
	global_load_dword v116, v[94:95], off offset:512
	global_load_dword v117, v[94:95], off offset:256
	global_load_dword v118, v[94:95], off
	s_waitcnt lgkmcnt(0)
	s_barrier
	ds_read_b128 v[94:97], v89
	ds_read_b128 v[98:101], v88
	ds_read_b128 v[102:105], v89 offset:32
	ds_read_b128 v[106:109], v88 offset:1024
	s_waitcnt lgkmcnt(0)
	v_mfma_f32_32x32x16_f16 v[2:17], v[94:97], v[106:109], v[2:17]
	s_mov_b32 s2, 0xe000
	v_add_co_u32_e32 v68, vcc, s2, v68
	v_cmp_eq_u32_e64 s[2:3], 1, v86
	s_nop 0
	v_addc_co_u32_e32 v69, vcc, 0, v69, vcc
	v_cmp_ne_u32_e32 vcc, 1, v86
	v_mfma_f32_32x32x16_f16 v[18:33], v[94:97], v[98:101], v[18:33]
	ds_read_b128 v[94:97], v88 offset:2048
	ds_read_b128 v[98:101], v88 offset:3072
	s_waitcnt vmcnt(12)
	s_waitcnt lgkmcnt(0)
	v_mfma_f32_32x32x16_f16 v[2:17], v[102:105], v[98:101], v[2:17]
	v_mov_b32_e32 v98, v51
	v_mov_b32_e32 v51, v53
	v_mov_b32_e32 v53, v57
	v_mov_b32_e32 v57, v65
	v_cvt_pk_f16_f32 v51, v52, v51
	v_cvt_pk_f16_f32 v50, v50, v98
	v_mfma_f32_32x32x16_f16 v[18:33], v[102:105], v[94:97], v[18:33]
	v_cvt_pk_f16_f32 v97, v110, v93
	v_cvt_pk_f16_f32 v96, v120, v119
	v_cvt_pk_f16_f32 v95, v122, v121
	v_cvt_pk_f16_f32 v94, v124, v123
	v_cvt_pk_f16_f32 v53, v56, v53
	v_cvt_pk_f16_f32 v52, v54, v55
	ds_write_b128 v87, v[94:97] offset:4096
	ds_write2_b64 v91, v[50:51], v[52:53] offset0:64 offset1:144
	v_cvt_pk_f16_f32 v51, v60, v61
	v_cvt_pk_f16_f32 v50, v58, v59
	v_cvt_pk_f16_f32 v53, v64, v57
	v_cvt_pk_f16_f32 v52, v62, v63
	ds_write2_b64 v92, v[50:51], v[52:53] offset0:96 offset1:176
	global_load_dwordx4 v[50:53], v[70:71], off offset:896
	global_load_dwordx4 v[54:57], v[72:73], off offset:896
	global_load_dwordx4 v[58:61], v[76:77], off offset:896
	global_load_dwordx4 v[62:65], v[74:75], off offset:896
	s_nop 0
	global_load_dword v76, v[68:69], off offset:1792
	global_load_dword v77, v[68:69], off offset:1536
	global_load_dword v93, v[68:69], off offset:1280
	global_load_dword v102, v[68:69], off offset:1024
	global_load_dword v103, v[68:69], off offset:768
	global_load_dword v104, v[68:69], off offset:512
	global_load_dword v105, v[68:69], off offset:256
	global_load_dword v106, v[68:69], off
	s_waitcnt lgkmcnt(0)
	s_barrier
	ds_read_b128 v[68:71], v89 offset:2560
	ds_read_b128 v[72:75], v88 offset:4096
	ds_read_b128 v[94:97], v89 offset:2592
	ds_read_b128 v[98:101], v88 offset:5120
	s_waitcnt lgkmcnt(2)
	v_mfma_f32_32x32x16_f16 v[18:33], v[68:71], v[72:75], v[18:33]
	s_waitcnt lgkmcnt(0)
	v_mfma_f32_32x32x16_f16 v[2:17], v[68:71], v[98:101], v[2:17]
	ds_read_b128 v[68:71], v88 offset:6144
	ds_read_b128 v[72:75], v88 offset:7168
	s_waitcnt vmcnt(12)
	s_waitcnt lgkmcnt(1)
	v_mfma_f32_32x32x16_f16 v[18:33], v[94:97], v[68:71], v[18:33]
	v_mov_b32_e32 v68, v37
	v_mov_b32_e32 v69, v39
	v_mov_b32_e32 v70, v36
	v_mov_b32_e32 v71, v38
	v_cvt_pk_f16_f32 v39, v112, v111
	v_cvt_pk_f16_f32 v38, v114, v113
	s_waitcnt lgkmcnt(0)
	v_mfma_f32_32x32x16_f16 v[2:17], v[94:97], v[72:75], v[2:17]
	v_cvt_pk_f16_f32 v37, v116, v115
	v_cvt_pk_f16_f32 v36, v118, v117
	ds_write_b128 v87, v[36:39]
	v_cvt_pk_f16_f32 v37, v70, v68
	v_cvt_pk_f16_f32 v36, v34, v35
	v_cvt_pk_f16_f32 v35, v40, v41
	v_cvt_pk_f16_f32 v34, v71, v69
	ds_write2_b64 v90, v[36:37], v[34:35] offset1:80
	v_cvt_pk_f16_f32 v35, v44, v45
	v_cvt_pk_f16_f32 v34, v42, v43
	v_cvt_pk_f16_f32 v37, v48, v49
	v_cvt_pk_f16_f32 v36, v46, v47
	ds_write2_b64 v90, v[34:35], v[36:37] offset0:160 offset1:240
	s_waitcnt lgkmcnt(0)
	s_barrier
	ds_read_b128 v[34:37], v89
	ds_read_b128 v[38:41], v88
	ds_read_b128 v[42:45], v89 offset:32
	ds_read_b128 v[46:49], v88 offset:1024
	s_waitcnt lgkmcnt(2)
	v_mfma_f32_32x32x16_f16 v[18:33], v[34:37], v[38:41], v[18:33]
	s_waitcnt lgkmcnt(0)
	v_mfma_f32_32x32x16_f16 v[2:17], v[34:37], v[46:49], v[2:17]
	ds_read_b128 v[34:37], v88 offset:2048
	ds_read_b128 v[38:41], v88 offset:3072
	s_waitcnt vmcnt(0)
	s_waitcnt lgkmcnt(1)
	v_mfma_f32_32x32x16_f16 v[18:33], v[42:45], v[34:37], v[18:33]
	v_mov_b32_e32 v46, v58
	v_mov_b32_e32 v47, v65
	v_mov_b32_e32 v48, v60
	v_mov_b32_e32 v49, v62
	v_cvt_pk_f16_f32 v37, v77, v76
	v_cvt_pk_f16_f32 v36, v102, v93
	v_cvt_pk_f16_f32 v35, v104, v103
	s_waitcnt lgkmcnt(0)
	v_mfma_f32_32x32x16_f16 v[2:17], v[42:45], v[38:41], v[2:17]
	v_mov_b32_e32 v38, v50
	v_mov_b32_e32 v39, v57
	v_mov_b32_e32 v40, v52
	v_mov_b32_e32 v41, v54
	v_mov_b32_e32 v42, v56
	v_mov_b32_e32 v43, v51
	v_mov_b32_e32 v44, v61
	v_mov_b32_e32 v45, v63
	v_cvt_pk_f16_f32 v34, v106, v105
	ds_write_b128 v87, v[34:37] offset:4096
	v_cvt_pk_f16_f32 v35, v40, v53
	v_cvt_pk_f16_f32 v34, v38, v43
	v_cvt_pk_f16_f32 v37, v42, v39
	v_cvt_pk_f16_f32 v36, v41, v55
	ds_write2_b64 v91, v[34:35], v[36:37] offset0:64 offset1:144
	v_cvt_pk_f16_f32 v35, v48, v44
	v_cvt_pk_f16_f32 v34, v46, v59
	v_cvt_pk_f16_f32 v37, v64, v47
	v_cvt_pk_f16_f32 v36, v49, v45
	ds_write2_b64 v92, v[34:35], v[36:37] offset0:96 offset1:176
	s_waitcnt lgkmcnt(0)
	s_barrier
	ds_read_b128 v[34:37], v89 offset:2560
	ds_read_b128 v[38:41], v88 offset:4096
	ds_read_b128 v[42:45], v89 offset:2592
	ds_read_b128 v[46:49], v88 offset:5120
	s_waitcnt lgkmcnt(2)
	v_mfma_f32_32x32x16_f16 v[18:33], v[34:37], v[38:41], v[18:33]
	s_waitcnt lgkmcnt(0)
	v_mfma_f32_32x32x16_f16 v[2:17], v[34:37], v[46:49], v[2:17]
	ds_read_b128 v[34:37], v88 offset:6144
	ds_read_b128 v[38:41], v88 offset:7168
	s_waitcnt lgkmcnt(0)
	s_barrier
	v_mfma_f32_32x32x16_f16 v[18:33], v[42:45], v[34:37], v[18:33]
	v_mfma_f32_32x32x16_f16 v[2:17], v[42:45], v[38:41], v[2:17]
	s_and_saveexec_b64 s[4:5], s[2:3]
	s_cbranch_execz .LBB0_2
	v_lshl_or_b32 v34, v85, 13, v66
	s_nop 7
	ds_write2st64_b32 v34, v18, v19 offset1:1
	ds_write2st64_b32 v34, v20, v21 offset0:2 offset1:3
	ds_write2st64_b32 v34, v22, v23 offset0:4 offset1:5
	ds_write2st64_b32 v34, v24, v25 offset0:6 offset1:7
	ds_write2st64_b32 v34, v26, v27 offset0:8 offset1:9
	ds_write2st64_b32 v34, v28, v29 offset0:10 offset1:11
	ds_write2st64_b32 v34, v30, v31 offset0:12 offset1:13
	ds_write2st64_b32 v34, v32, v33 offset0:14 offset1:15
	ds_write2st64_b32 v34, v2, v3 offset0:16 offset1:17
	ds_write2st64_b32 v34, v4, v5 offset0:18 offset1:19
	ds_write2st64_b32 v34, v6, v7 offset0:20 offset1:21
	ds_write2st64_b32 v34, v8, v9 offset0:22 offset1:23
	ds_write2st64_b32 v34, v10, v11 offset0:24 offset1:25
	ds_write2st64_b32 v34, v12, v13 offset0:26 offset1:27
	ds_write2st64_b32 v34, v14, v15 offset0:28 offset1:29
	ds_write2st64_b32 v34, v16, v17 offset0:30 offset1:31
